# combo7 + phase 0: w_in column-max loops issue 16 loads per round trip (two trips merged); rows per workgroup 37 / 104
# baseline (speedup 1.0000x reference)
.LBB0_9:
	v_lshl_add_u64 v[36:37], v[22:23], 0, s[6:7]
	v_add_co_u32_e32 v28, vcc, 0x9000, v36
	global_load_dwordx4 v[80:83], v[36:37], off
	s_nop 0
	v_addc_co_u32_e32 v29, vcc, 0, v37, vcc
	v_add_co_u32_e32 v46, vcc, 0x13000, v36
	global_load_dwordx4 v[84:87], v[28:29], off offset:2080
	s_nop 0
	v_addc_co_u32_e32 v47, vcc, 0, v37, vcc
	v_add_co_u32_e32 v48, vcc, 0x1c000, v36
	s_add_u32 s6, s6, 0x260800
	s_nop 0
	v_addc_co_u32_e32 v49, vcc, 0, v37, vcc
	v_add_co_u32_e32 v54, vcc, 0x26000, v36
	global_load_dwordx4 v[88:91], v[46:47], off offset:64
	global_load_dwordx4 v[92:95], v[48:49], off offset:2144
	v_addc_co_u32_e32 v55, vcc, 0, v37, vcc
	v_add_co_u32_e32 v56, vcc, 0x2f000, v36
	s_addc_u32 s7, s7, 0
	s_nop 0
	v_addc_co_u32_e32 v57, vcc, 0, v37, vcc
	v_add_co_u32_e32 v62, vcc, 0x39000, v36
	global_load_dwordx4 v[96:99], v[54:55], off offset:128
	global_load_dwordx4 v[100:103], v[56:57], off offset:2208
	v_addc_co_u32_e32 v63, vcc, 0, v37, vcc
	v_add_co_u32_e32 v36, vcc, 0x42000, v36
	s_nop 0
	v_addc_co_u32_e32 v37, vcc, 0, v37, vcc
	global_load_dwordx4 v[104:107], v[62:63], off offset:192
	global_load_dwordx4 v[108:111], v[36:37], off offset:2272
	v_lshl_add_u64 v[36:37], v[22:23], 0, s[6:7]
	v_add_co_u32_e32 v28, vcc, 0x9000, v36
	global_load_dwordx4 v[112:115], v[36:37], off
	s_nop 0
	v_addc_co_u32_e32 v29, vcc, 0, v37, vcc
	v_add_co_u32_e32 v46, vcc, 0x13000, v36
	global_load_dwordx4 v[116:119], v[28:29], off offset:2080
	s_nop 0
	v_addc_co_u32_e32 v47, vcc, 0, v37, vcc
	v_add_co_u32_e32 v48, vcc, 0x1c000, v36
	s_add_u32 s6, s6, 0x260800
	s_nop 0
	v_addc_co_u32_e32 v49, vcc, 0, v37, vcc
	v_add_co_u32_e32 v54, vcc, 0x26000, v36
	global_load_dwordx4 v[120:123], v[46:47], off offset:64
	global_load_dwordx4 v[124:127], v[48:49], off offset:2144
	v_addc_co_u32_e32 v55, vcc, 0, v37, vcc
	v_add_co_u32_e32 v56, vcc, 0x2f000, v36
	s_addc_u32 s7, s7, 0
	s_nop 0
	v_addc_co_u32_e32 v57, vcc, 0, v37, vcc
	v_add_co_u32_e32 v62, vcc, 0x39000, v36
	global_load_dwordx4 v[128:131], v[54:55], off offset:128
	global_load_dwordx4 v[132:135], v[56:57], off offset:2208
	v_addc_co_u32_e32 v63, vcc, 0, v37, vcc
	v_add_co_u32_e32 v36, vcc, 0x42000, v36
	s_nop 0
	v_addc_co_u32_e32 v37, vcc, 0, v37, vcc
	global_load_dwordx4 v[136:139], v[62:63], off offset:192
	global_load_dwordx4 v[140:143], v[36:37], off offset:2272
	s_waitcnt vmcnt(14)
	v_max3_f32 v9, v13, |v80|, |v84|
	v_max3_f32 v11, v19, |v81|, |v85|
	v_max3_f32 v13, v17, |v82|, |v86|
	v_max3_f32 v15, v15, |v83|, |v87|
	s_waitcnt vmcnt(12)
	v_max3_f32 v9, v9, |v88|, |v92|
	v_max3_f32 v11, v11, |v89|, |v93|
	v_max3_f32 v13, v13, |v90|, |v94|
	v_max3_f32 v15, v15, |v91|, |v95|
	s_waitcnt vmcnt(10)
	v_max3_f32 v9, v9, |v96|, |v100|
	v_max3_f32 v11, v11, |v97|, |v101|
	v_max3_f32 v17, v13, |v98|, |v102|
	v_max3_f32 v15, v15, |v99|, |v103|
	s_waitcnt vmcnt(8)
	v_max3_f32 v13, v9, |v104|, |v108|
	v_max3_f32 v19, v11, |v105|, |v109|
	v_max3_f32 v17, v17, |v106|, |v110|
	v_max3_f32 v15, v15, |v107|, |v111|
	s_waitcnt vmcnt(6)
	v_max3_f32 v9, v13, |v112|, |v116|
	v_max3_f32 v11, v19, |v113|, |v117|
	v_max3_f32 v13, v17, |v114|, |v118|
	v_max3_f32 v15, v15, |v115|, |v119|
	s_waitcnt vmcnt(4)
	v_max3_f32 v9, v9, |v120|, |v124|
	v_max3_f32 v11, v11, |v121|, |v125|
	v_max3_f32 v13, v13, |v122|, |v126|
	v_max3_f32 v15, v15, |v123|, |v127|
	s_waitcnt vmcnt(2)
	v_max3_f32 v9, v9, |v128|, |v132|
	v_max3_f32 v11, v11, |v129|, |v133|
	v_max3_f32 v17, v13, |v130|, |v134|
	v_max3_f32 v15, v15, |v131|, |v135|
	s_waitcnt vmcnt(0)
	v_max3_f32 v13, v9, |v136|, |v140|
	v_max3_f32 v19, v11, |v137|, |v141|
	v_max3_f32 v17, v17, |v138|, |v142|
	v_max3_f32 v15, v15, |v139|, |v143|
	v_lshl_add_u64 v[36:37], v[22:23], 0, s[6:7]
	v_add_co_u32_e32 v28, vcc, 0x9000, v36
	global_load_dwordx4 v[80:83], v[36:37], off
	s_nop 0
	v_addc_co_u32_e32 v29, vcc, 0, v37, vcc
	v_add_co_u32_e32 v46, vcc, 0x13000, v36
	global_load_dwordx4 v[84:87], v[28:29], off offset:2080
	s_nop 0
	v_addc_co_u32_e32 v47, vcc, 0, v37, vcc
	v_add_co_u32_e32 v48, vcc, 0x1c000, v36
	s_add_u32 s6, s6, 0x260800
	s_nop 0
	v_addc_co_u32_e32 v49, vcc, 0, v37, vcc
	v_add_co_u32_e32 v54, vcc, 0x26000, v36
	global_load_dwordx4 v[88:91], v[46:47], off offset:64
	global_load_dwordx4 v[92:95], v[48:49], off offset:2144
	v_addc_co_u32_e32 v55, vcc, 0, v37, vcc
	v_add_co_u32_e32 v56, vcc, 0x2f000, v36
	s_addc_u32 s7, s7, 0
	s_nop 0
	v_addc_co_u32_e32 v57, vcc, 0, v37, vcc
	v_add_co_u32_e32 v62, vcc, 0x39000, v36
	global_load_dwordx4 v[96:99], v[54:55], off offset:128
	global_load_dwordx4 v[100:103], v[56:57], off offset:2208
	v_addc_co_u32_e32 v63, vcc, 0, v37, vcc
	v_add_co_u32_e32 v36, vcc, 0x42000, v36
	s_nop 0
	v_addc_co_u32_e32 v37, vcc, 0, v37, vcc
	global_load_dwordx4 v[104:107], v[62:63], off offset:192
	global_load_dwordx4 v[108:111], v[36:37], off offset:2272
	v_lshl_add_u64 v[36:37], v[22:23], 0, s[6:7]
	v_add_co_u32_e32 v28, vcc, 0x9000, v36
	global_load_dwordx4 v[112:115], v[36:37], off
	s_nop 0
	v_addc_co_u32_e32 v29, vcc, 0, v37, vcc
	v_add_co_u32_e32 v46, vcc, 0x13000, v36
	global_load_dwordx4 v[116:119], v[28:29], off offset:2080
	s_nop 0
	v_addc_co_u32_e32 v47, vcc, 0, v37, vcc
	v_add_co_u32_e32 v48, vcc, 0x1c000, v36
	s_add_u32 s6, s6, 0x260800
	s_nop 0
	v_addc_co_u32_e32 v49, vcc, 0, v37, vcc
	v_add_co_u32_e32 v54, vcc, 0x26000, v36
	global_load_dwordx4 v[120:123], v[46:47], off offset:64
	global_load_dwordx4 v[124:127], v[48:49], off offset:2144
	v_addc_co_u32_e32 v55, vcc, 0, v37, vcc
	v_add_co_u32_e32 v56, vcc, 0x2f000, v36
	s_addc_u32 s7, s7, 0
	s_nop 0
	v_addc_co_u32_e32 v57, vcc, 0, v37, vcc
	v_add_co_u32_e32 v62, vcc, 0x39000, v36
	global_load_dwordx4 v[128:131], v[54:55], off offset:128
	global_load_dwordx4 v[132:135], v[56:57], off offset:2208
	v_addc_co_u32_e32 v63, vcc, 0, v37, vcc
	v_add_co_u32_e32 v36, vcc, 0x42000, v36
	s_nop 0
	v_addc_co_u32_e32 v37, vcc, 0, v37, vcc
	global_load_dwordx4 v[136:139], v[62:63], off offset:192
	global_load_dwordx4 v[140:143], v[36:37], off offset:2272
	s_waitcnt vmcnt(14)
	v_max3_f32 v9, v13, |v80|, |v84|
	v_max3_f32 v11, v19, |v81|, |v85|
	v_max3_f32 v13, v17, |v82|, |v86|
	v_max3_f32 v15, v15, |v83|, |v87|
	s_waitcnt vmcnt(12)
	v_max3_f32 v9, v9, |v88|, |v92|
	v_max3_f32 v11, v11, |v89|, |v93|
	v_max3_f32 v13, v13, |v90|, |v94|
	v_max3_f32 v15, v15, |v91|, |v95|
	s_waitcnt vmcnt(10)
	v_max3_f32 v9, v9, |v96|, |v100|
	v_max3_f32 v11, v11, |v97|, |v101|
	v_max3_f32 v17, v13, |v98|, |v102|
	v_max3_f32 v15, v15, |v99|, |v103|
	s_waitcnt vmcnt(8)
	v_max3_f32 v13, v9, |v104|, |v108|
	v_max3_f32 v19, v11, |v105|, |v109|
	v_max3_f32 v17, v17, |v106|, |v110|
	v_max3_f32 v15, v15, |v107|, |v111|
	s_waitcnt vmcnt(6)
	v_max3_f32 v9, v13, |v112|, |v116|
	v_max3_f32 v11, v19, |v113|, |v117|
	v_max3_f32 v13, v17, |v114|, |v118|
	v_max3_f32 v15, v15, |v115|, |v119|
	s_waitcnt vmcnt(4)
	v_max3_f32 v9, v9, |v120|, |v124|
	v_max3_f32 v11, v11, |v121|, |v125|
	v_max3_f32 v13, v13, |v122|, |v126|
	v_max3_f32 v15, v15, |v123|, |v127|
	s_waitcnt vmcnt(2)
	v_max3_f32 v9, v9, |v128|, |v132|
	v_max3_f32 v11, v11, |v129|, |v133|
	v_max3_f32 v17, v13, |v130|, |v134|
	v_max3_f32 v15, v15, |v131|, |v135|
	s_waitcnt vmcnt(0)
	v_max3_f32 v13, v9, |v136|, |v140|
	v_max3_f32 v19, v11, |v137|, |v141|
	v_max3_f32 v17, v17, |v138|, |v142|
	v_max3_f32 v15, v15, |v139|, |v143|
	v_and_b32_e32 v11, 64, v40
	v_xor_b32_e32 v9, 8, v40
	v_add_u32_e32 v21, 64, v11
	v_cmp_lt_i32_e32 vcc, v9, v21
	v_xor_b32_e32 v11, 16, v40
	s_nop 0
	v_cndmask_b32_e32 v9, v40, v9, vcc
	v_lshlrev_b32_e32 v9, 2, v9
	ds_bpermute_b32 v24, v9, v13
	v_cmp_lt_i32_e32 vcc, v11, v21
	v_max_f32_e32 v13, v13, v13
	s_waitcnt lgkmcnt(0)
	v_max_f32_e32 v24, v24, v24
	v_cndmask_b32_e32 v11, v40, v11, vcc
	v_lshlrev_b32_e32 v11, 2, v11
	v_max_f32_e32 v24, v13, v24
	ds_bpermute_b32 v25, v11, v24
	v_xor_b32_e32 v13, 32, v40
	v_cmp_lt_i32_e32 vcc, v13, v21
	s_waitcnt lgkmcnt(0)
	v_max_f32_e32 v21, v25, v25
	v_cndmask_b32_e32 v13, v40, v13, vcc
	v_lshlrev_b32_e32 v13, 2, v13
	v_max_f32_e32 v21, v24, v21
	ds_bpermute_b32 v24, v13, v21
	s_and_saveexec_b64 s[6:7], s[4:5]
	s_cbranch_execz .LBB0_12
	s_waitcnt lgkmcnt(0)
	v_max_f32_e32 v24, v24, v24
	v_max_f32_e32 v21, v21, v21
	v_max_f32_e32 v21, v21, v24
	ds_write_b32 v39, v21

.LBB0_19:
	v_lshl_add_u64 v[36:37], v[22:23], 0, s[6:7]
	v_add_co_u32_e32 v28, vcc, 0x9000, v36
	global_load_dwordx4 v[80:83], v[36:37], off offset:128
	s_nop 0
	v_addc_co_u32_e32 v29, vcc, 0, v37, vcc
	v_add_co_u32_e32 v46, vcc, 0x13000, v36
	global_load_dwordx4 v[84:87], v[28:29], off offset:2208
	s_nop 0
	v_addc_co_u32_e32 v47, vcc, 0, v37, vcc
	v_add_co_u32_e32 v48, vcc, 0x1c000, v36
	s_add_u32 s6, s6, 0x260800
	s_nop 0
	v_addc_co_u32_e32 v49, vcc, 0, v37, vcc
	v_add_co_u32_e32 v54, vcc, 0x26000, v36
	global_load_dwordx4 v[88:91], v[46:47], off offset:192
	global_load_dwordx4 v[92:95], v[48:49], off offset:2272
	v_addc_co_u32_e32 v55, vcc, 0, v37, vcc
	v_add_co_u32_e32 v56, vcc, 0x2f000, v36
	s_addc_u32 s7, s7, 0
	s_nop 0
	v_addc_co_u32_e32 v57, vcc, 0, v37, vcc
	v_add_co_u32_e32 v62, vcc, 0x39000, v36
	global_load_dwordx4 v[96:99], v[54:55], off offset:256
	global_load_dwordx4 v[100:103], v[56:57], off offset:2336
	v_addc_co_u32_e32 v63, vcc, 0, v37, vcc
	v_add_co_u32_e32 v36, vcc, 0x42000, v36
	s_nop 0
	v_addc_co_u32_e32 v37, vcc, 0, v37, vcc
	global_load_dwordx4 v[104:107], v[62:63], off offset:320
	global_load_dwordx4 v[108:111], v[36:37], off offset:2400
	v_lshl_add_u64 v[36:37], v[22:23], 0, s[6:7]
	v_add_co_u32_e32 v28, vcc, 0x9000, v36
	global_load_dwordx4 v[112:115], v[36:37], off offset:128
	s_nop 0
	v_addc_co_u32_e32 v29, vcc, 0, v37, vcc
	v_add_co_u32_e32 v46, vcc, 0x13000, v36
	global_load_dwordx4 v[116:119], v[28:29], off offset:2208
	s_nop 0
	v_addc_co_u32_e32 v47, vcc, 0, v37, vcc
	v_add_co_u32_e32 v48, vcc, 0x1c000, v36
	s_add_u32 s6, s6, 0x260800
	s_nop 0
	v_addc_co_u32_e32 v49, vcc, 0, v37, vcc
	v_add_co_u32_e32 v54, vcc, 0x26000, v36
	global_load_dwordx4 v[120:123], v[46:47], off offset:192
	global_load_dwordx4 v[124:127], v[48:49], off offset:2272
	v_addc_co_u32_e32 v55, vcc, 0, v37, vcc
	v_add_co_u32_e32 v56, vcc, 0x2f000, v36
	s_addc_u32 s7, s7, 0
	s_nop 0
	v_addc_co_u32_e32 v57, vcc, 0, v37, vcc
	v_add_co_u32_e32 v62, vcc, 0x39000, v36
	global_load_dwordx4 v[128:131], v[54:55], off offset:256
	global_load_dwordx4 v[132:135], v[56:57], off offset:2336
	v_addc_co_u32_e32 v63, vcc, 0, v37, vcc
	v_add_co_u32_e32 v36, vcc, 0x42000, v36
	s_nop 0
	v_addc_co_u32_e32 v37, vcc, 0, v37, vcc
	global_load_dwordx4 v[136:139], v[62:63], off offset:320
	global_load_dwordx4 v[140:143], v[36:37], off offset:2400
	s_waitcnt vmcnt(14)
	v_max3_f32 v21, v21, |v80|, |v84|
	v_max3_f32 v19, v19, |v81|, |v85|
	v_max3_f32 v17, v17, |v82|, |v86|
	v_max3_f32 v15, v15, |v83|, |v87|
	s_waitcnt vmcnt(12)
	v_max3_f32 v21, v21, |v88|, |v92|
	v_max3_f32 v19, v19, |v89|, |v93|
	v_max3_f32 v17, v17, |v90|, |v94|
	v_max3_f32 v15, v15, |v91|, |v95|
	s_waitcnt vmcnt(10)
	v_max3_f32 v21, v21, |v96|, |v100|
	v_max3_f32 v19, v19, |v97|, |v101|
	v_max3_f32 v17, v17, |v98|, |v102|
	v_max3_f32 v15, v15, |v99|, |v103|
	s_waitcnt vmcnt(8)
	v_max3_f32 v21, v21, |v104|, |v108|
	v_max3_f32 v19, v19, |v105|, |v109|
	v_max3_f32 v17, v17, |v106|, |v110|
	v_max3_f32 v15, v15, |v107|, |v111|
	s_waitcnt vmcnt(6)
	v_max3_f32 v21, v21, |v112|, |v116|
	v_max3_f32 v19, v19, |v113|, |v117|
	v_max3_f32 v17, v17, |v114|, |v118|
	v_max3_f32 v15, v15, |v115|, |v119|
	s_waitcnt vmcnt(4)
	v_max3_f32 v21, v21, |v120|, |v124|
	v_max3_f32 v19, v19, |v121|, |v125|
	v_max3_f32 v17, v17, |v122|, |v126|
	v_max3_f32 v15, v15, |v123|, |v127|
	s_waitcnt vmcnt(2)
	v_max3_f32 v21, v21, |v128|, |v132|
	v_max3_f32 v19, v19, |v129|, |v133|
	v_max3_f32 v17, v17, |v130|, |v134|
	v_max3_f32 v15, v15, |v131|, |v135|
	s_waitcnt vmcnt(0)
	v_max3_f32 v21, v21, |v136|, |v140|
	v_max3_f32 v19, v19, |v137|, |v141|
	v_max3_f32 v17, v17, |v138|, |v142|
	v_max3_f32 v15, v15, |v139|, |v143|
	v_lshl_add_u64 v[36:37], v[22:23], 0, s[6:7]
	v_add_co_u32_e32 v28, vcc, 0x9000, v36
	global_load_dwordx4 v[80:83], v[36:37], off offset:128
	s_nop 0
	v_addc_co_u32_e32 v29, vcc, 0, v37, vcc
	v_add_co_u32_e32 v46, vcc, 0x13000, v36
	global_load_dwordx4 v[84:87], v[28:29], off offset:2208
	s_nop 0
	v_addc_co_u32_e32 v47, vcc, 0, v37, vcc
	v_add_co_u32_e32 v48, vcc, 0x1c000, v36
	s_add_u32 s6, s6, 0x260800
	s_nop 0
	v_addc_co_u32_e32 v49, vcc, 0, v37, vcc
	v_add_co_u32_e32 v54, vcc, 0x26000, v36
	global_load_dwordx4 v[88:91], v[46:47], off offset:192
	global_load_dwordx4 v[92:95], v[48:49], off offset:2272
	v_addc_co_u32_e32 v55, vcc, 0, v37, vcc
	v_add_co_u32_e32 v56, vcc, 0x2f000, v36
	s_addc_u32 s7, s7, 0
	s_nop 0
	v_addc_co_u32_e32 v57, vcc, 0, v37, vcc
	v_add_co_u32_e32 v62, vcc, 0x39000, v36
	global_load_dwordx4 v[96:99], v[54:55], off offset:256
	global_load_dwordx4 v[100:103], v[56:57], off offset:2336
	v_addc_co_u32_e32 v63, vcc, 0, v37, vcc
	v_add_co_u32_e32 v36, vcc, 0x42000, v36
	s_nop 0
	v_addc_co_u32_e32 v37, vcc, 0, v37, vcc
	global_load_dwordx4 v[104:107], v[62:63], off offset:320
	global_load_dwordx4 v[108:111], v[36:37], off offset:2400
	v_lshl_add_u64 v[36:37], v[22:23], 0, s[6:7]
	v_add_co_u32_e32 v28, vcc, 0x9000, v36
	global_load_dwordx4 v[112:115], v[36:37], off offset:128
	s_nop 0
	v_addc_co_u32_e32 v29, vcc, 0, v37, vcc
	v_add_co_u32_e32 v46, vcc, 0x13000, v36
	global_load_dwordx4 v[116:119], v[28:29], off offset:2208
	s_nop 0
	v_addc_co_u32_e32 v47, vcc, 0, v37, vcc
	v_add_co_u32_e32 v48, vcc, 0x1c000, v36
	s_add_u32 s6, s6, 0x260800
	s_nop 0
	v_addc_co_u32_e32 v49, vcc, 0, v37, vcc
	v_add_co_u32_e32 v54, vcc, 0x26000, v36
	global_load_dwordx4 v[120:123], v[46:47], off offset:192
	global_load_dwordx4 v[124:127], v[48:49], off offset:2272
	v_addc_co_u32_e32 v55, vcc, 0, v37, vcc
	v_add_co_u32_e32 v56, vcc, 0x2f000, v36
	s_addc_u32 s7, s7, 0
	s_nop 0
	v_addc_co_u32_e32 v57, vcc, 0, v37, vcc
	v_add_co_u32_e32 v62, vcc, 0x39000, v36
	global_load_dwordx4 v[128:131], v[54:55], off offset:256
	global_load_dwordx4 v[132:135], v[56:57], off offset:2336
	v_addc_co_u32_e32 v63, vcc, 0, v37, vcc
	v_add_co_u32_e32 v36, vcc, 0x42000, v36
	s_nop 0
	v_addc_co_u32_e32 v37, vcc, 0, v37, vcc
	global_load_dwordx4 v[136:139], v[62:63], off offset:320
	global_load_dwordx4 v[140:143], v[36:37], off offset:2400
	s_waitcnt vmcnt(14)
	v_max3_f32 v21, v21, |v80|, |v84|
	v_max3_f32 v19, v19, |v81|, |v85|
	v_max3_f32 v17, v17, |v82|, |v86|
	v_max3_f32 v15, v15, |v83|, |v87|
	s_waitcnt vmcnt(12)
	v_max3_f32 v21, v21, |v88|, |v92|
	v_max3_f32 v19, v19, |v89|, |v93|
	v_max3_f32 v17, v17, |v90|, |v94|
	v_max3_f32 v15, v15, |v91|, |v95|
	s_waitcnt vmcnt(10)
	v_max3_f32 v21, v21, |v96|, |v100|
	v_max3_f32 v19, v19, |v97|, |v101|
	v_max3_f32 v17, v17, |v98|, |v102|
	v_max3_f32 v15, v15, |v99|, |v103|
	s_waitcnt vmcnt(8)
	v_max3_f32 v21, v21, |v104|, |v108|
	v_max3_f32 v19, v19, |v105|, |v109|
	v_max3_f32 v17, v17, |v106|, |v110|
	v_max3_f32 v15, v15, |v107|, |v111|
	s_waitcnt vmcnt(6)
	v_max3_f32 v21, v21, |v112|, |v116|
	v_max3_f32 v19, v19, |v113|, |v117|
	v_max3_f32 v17, v17, |v114|, |v118|
	v_max3_f32 v15, v15, |v115|, |v119|
	s_waitcnt vmcnt(4)
	v_max3_f32 v21, v21, |v120|, |v124|
	v_max3_f32 v19, v19, |v121|, |v125|
	v_max3_f32 v17, v17, |v122|, |v126|
	v_max3_f32 v15, v15, |v123|, |v127|
	s_waitcnt vmcnt(2)
	v_max3_f32 v21, v21, |v128|, |v132|
	v_max3_f32 v19, v19, |v129|, |v133|
	v_max3_f32 v17, v17, |v130|, |v134|
	v_max3_f32 v15, v15, |v131|, |v135|
	s_waitcnt vmcnt(0)
	v_max3_f32 v21, v21, |v136|, |v140|
	v_max3_f32 v19, v19, |v137|, |v141|
	v_max3_f32 v17, v17, |v138|, |v142|
	v_max3_f32 v15, v15, |v139|, |v143|
	ds_bpermute_b32 v24, v9, v21
	v_max_f32_e32 v21, v21, v21
	s_waitcnt lgkmcnt(0)
	v_max_f32_e32 v24, v24, v24
	v_max_f32_e32 v21, v21, v24
	ds_bpermute_b32 v24, v11, v21
	s_waitcnt lgkmcnt(0)
	v_max_f32_e32 v24, v24, v24
	v_max_f32_e32 v21, v21, v24
	ds_bpermute_b32 v24, v13, v21
	s_and_saveexec_b64 s[6:7], s[4:5]
	s_cbranch_execz .LBB0_22
	s_waitcnt lgkmcnt(0)
	v_max_f32_e32 v24, v24, v24
	v_max_f32_e32 v21, v21, v21
	v_max_f32_e32 v21, v21, v24
	ds_write_b32 v39, v21 offset:128
